# gemm_gu first-unit row gathers batched; POS fix-up loads hoisted to phase start; router tail loads overlap the CNT atomic
# speedup vs baseline: 1.0560x; 1.0005x over previous
.LBB0_1420:
	s_waitcnt vmcnt(0) lgkmcnt(0)
	s_barrier
	v_lshrrev_b32_e32 v2, 6, v14
	v_mul_lo_u32 v2, v2, s95
	v_add_u32_e32 v2, s97, v2
	s_lshr_b32 s6, s30, 4
	v_cmp_gt_u32_e32 vcc, s6, v2
	v_and_b32_e32 v3, 63, v14
	v_lshl_or_b32 v2, v2, 6, v3
	s_add_u32 s2, s16, 0x2bb88000
	s_addc_u32 s3, s17, 0
	v_cndmask_b32_e32 v3, 0, v2, vcc
	s_add_u32 s4, s16, 0x2bbcc000
	s_addc_u32 s5, s17, 0
	v_lshlrev_b32_e32 v3, 2, v3
	global_load_dword v4, v3, s[2:3] sc1
	global_load_dword v5, v3, s[4:5] sc1
	v_cmp_gt_u32_e32 vcc, 32, v14
	s_and_saveexec_b64 s[0:1], vcc
	s_cbranch_execz .Lmy_rt_a
	v_add_u32_e32 v10, 0x20840, v1
	ds_read_b32 v11, v10
	v_readlane_b32 s2, v255, 37
	s_mov_b32 s3, 0
	s_lshl_b32 s2, s2, 6
	s_lshl_b64 s[2:3], s[2:3], 2
	s_add_u32 s2, s16, s2
	s_addc_u32 s3, s17, s3
	v_ashrrev_i32_e32 v15, 31, v14
	v_lshl_add_u64 v[8:9], v[14:15], 2, s[2:3]
	v_add_co_u32_e32 v8, vcc, 0x10000, v8
	s_nop 1
	v_addc_co_u32_e32 v9, vcc, 0, v9, vcc
	v_add_u32_e32 v13, 0x20c40, v1
	ds_write_b32 v13, v35
	s_waitcnt lgkmcnt(0)
	global_atomic_add v12, v[8:9], v11, off sc0
	v_add_u32_e32 v13, 0x20b40, v1
	s_waitcnt vmcnt(0)
	ds_write_b32 v13, v12
.Lmy_rt_a:
	s_or_b64 exec, exec, s[0:1]
	s_waitcnt vmcnt(0) lgkmcnt(0)
	s_barrier
	v_lshrrev_b32_e32 v6, 6, v2
	v_cmp_gt_u32_e32 vcc, s6, v6
	s_and_saveexec_b64 s[0:1], vcc
	s_cbranch_execz .Lmy_rt_b
	v_lshlrev_b32_e32 v6, 2, v4
	v_add_u32_e32 v7, 0x20b40, v6
	v_add_u32_e32 v8, 0x20c40, v6
	ds_read_b32 v7, v7
	ds_add_rtn_u32 v8, v8, v250
	s_add_u32 s6, s16, 0x2bc10000
	s_addc_u32 s7, s17, 0
	s_add_u32 s8, s16, 0xd5f8000
	s_addc_u32 s9, s17, 0
	s_add_u32 s10, s16, 0xd818000
	s_addc_u32 s11, s17, 0
	v_mul_u32_u24_e32 v9, 0x4400, v4
	v_lshrrev_b32_e32 v10, 2, v2
	s_waitcnt lgkmcnt(0)
	v_add_u32_e32 v7, v7, v8
	global_store_dword v3, v7, s[6:7]
	v_add_lshl_u32 v9, v9, v7, 2
	global_store_dword v9, v10, s[8:9]
	global_store_dword v9, v5, s[10:11]

.LBB0_1561:
	s_andn2_b64 vcc, exec, s[0:1]
	s_cbranch_vccnz .LBB0_1641
	v_mov_b32_e32 v2, v0
	s_nop 0
	s_mul_i32 s0, s97, 0x110
	v_add_u32_e32 v7, s0, v2
	s_lshl_b32 s0, s30, 2
	v_cmp_gt_u32_e32 vcc, s0, v7
	s_add_u32 s4, s16, 0x2bb88000
	s_addc_u32 s5, s17, 0
	v_cndmask_b32_e32 v7, 0, v7, vcc
	s_add_u32 s6, s16, 0x2bc10000
	s_addc_u32 s7, s17, 0
	v_lshlrev_b32_e32 v7, 2, v7
	global_load_dword v8, v7, s[4:5]
	global_load_dword v9, v7, s[6:7]
	v_cmp_gt_i32_e32 vcc, 32, v2
	s_and_saveexec_b64 s[2:3], vcc
	v_readlane_b32 s10, v255, 16
	v_readlane_b32 s11, v255, 17
	v_readlane_b32 s14, v255, 18
	s_cbranch_execz .LBB0_1574
	v_mov_b32_e32 v1, 0
	s_mov_b64 s[4:5], exec
	v_readlane_b32 s6, v255, 25
	v_readlane_b32 s7, v255, 26
	s_add_u32 s6, s16, s6
	s_addc_u32 s7, s17, s7
	v_lshlrev_b32_e32 v4, 2, v2
	global_load_dword v6, v4, s[6:7]
	s_mov_b32 s8, 0
	s_waitcnt vmcnt(0)
	v_add_u32_e32 v6, 0xff, v6
	v_and_b32_e32 v6, 0xffffff00, v6
	s_nop 1
	v_readlane_b32 s9, v6, 0
	s_add_u32 s8, s8, s9
	v_writelane_b32 v1, s8, 1
	v_readlane_b32 s9, v6, 1
	s_add_u32 s8, s8, s9
	v_writelane_b32 v1, s8, 2
	v_readlane_b32 s9, v6, 2
	s_add_u32 s8, s8, s9
	v_writelane_b32 v1, s8, 3
	v_readlane_b32 s9, v6, 3
	s_add_u32 s8, s8, s9
	v_writelane_b32 v1, s8, 4
	v_readlane_b32 s9, v6, 4
	s_add_u32 s8, s8, s9
	v_writelane_b32 v1, s8, 5
	v_readlane_b32 s9, v6, 5
	s_add_u32 s8, s8, s9
	v_writelane_b32 v1, s8, 6
	v_readlane_b32 s9, v6, 6
	s_add_u32 s8, s8, s9
	v_writelane_b32 v1, s8, 7
	v_readlane_b32 s9, v6, 7
	s_add_u32 s8, s8, s9
	v_writelane_b32 v1, s8, 8
	v_readlane_b32 s9, v6, 8
	s_add_u32 s8, s8, s9
	v_writelane_b32 v1, s8, 9
	v_readlane_b32 s9, v6, 9
	s_add_u32 s8, s8, s9
	v_writelane_b32 v1, s8, 10
	v_readlane_b32 s9, v6, 10
	s_add_u32 s8, s8, s9
	v_writelane_b32 v1, s8, 11
	v_readlane_b32 s9, v6, 11
	s_add_u32 s8, s8, s9
	v_writelane_b32 v1, s8, 12
	v_readlane_b32 s9, v6, 12
	s_add_u32 s8, s8, s9
	v_writelane_b32 v1, s8, 13
	v_readlane_b32 s9, v6, 13
	s_add_u32 s8, s8, s9
	v_writelane_b32 v1, s8, 14
	v_readlane_b32 s9, v6, 14
	s_add_u32 s8, s8, s9
	v_writelane_b32 v1, s8, 15
	v_readlane_b32 s9, v6, 15
	s_add_u32 s8, s8, s9
	v_writelane_b32 v1, s8, 16
	v_readlane_b32 s9, v6, 16
	s_add_u32 s8, s8, s9
	v_writelane_b32 v1, s8, 17
	v_readlane_b32 s9, v6, 17
	s_add_u32 s8, s8, s9
	v_writelane_b32 v1, s8, 18
	v_readlane_b32 s9, v6, 18
	s_add_u32 s8, s8, s9
	v_writelane_b32 v1, s8, 19
	v_readlane_b32 s9, v6, 19
	s_add_u32 s8, s8, s9
	v_writelane_b32 v1, s8, 20
	v_readlane_b32 s9, v6, 20
	s_add_u32 s8, s8, s9
	v_writelane_b32 v1, s8, 21
	v_readlane_b32 s9, v6, 21
	s_add_u32 s8, s8, s9
	v_writelane_b32 v1, s8, 22
	v_readlane_b32 s9, v6, 22
	s_add_u32 s8, s8, s9
	v_writelane_b32 v1, s8, 23
	v_readlane_b32 s9, v6, 23
	s_add_u32 s8, s8, s9
	v_writelane_b32 v1, s8, 24
	v_readlane_b32 s9, v6, 24
	s_add_u32 s8, s8, s9
	v_writelane_b32 v1, s8, 25
	v_readlane_b32 s9, v6, 25
	s_add_u32 s8, s8, s9
	v_writelane_b32 v1, s8, 26
	v_readlane_b32 s9, v6, 26
	s_add_u32 s8, s8, s9
	v_writelane_b32 v1, s8, 27
	v_readlane_b32 s9, v6, 27
	s_add_u32 s8, s8, s9
	v_writelane_b32 v1, s8, 28
	v_readlane_b32 s9, v6, 28
	s_add_u32 s8, s8, s9
	v_writelane_b32 v1, s8, 29
	v_readlane_b32 s9, v6, 29
	s_add_u32 s8, s8, s9
	v_writelane_b32 v1, s8, 30
	v_readlane_b32 s9, v6, 30
	s_add_u32 s8, s8, s9
	v_writelane_b32 v1, s8, 31

.LBB0_1577:
	s_or_b64 exec, exec, s[2:3]
	v_cmp_gt_u32_e32 vcc, 0x110, v2
	s_and_saveexec_b64 s[2:3], vcc
	s_cbranch_execz .Lmy_pf_a
	s_mul_i32 s0, s97, 0x110
	v_add_u32_e32 v3, s0, v2
	s_lshl_b32 s0, s30, 2
	v_cmp_gt_u32_e32 vcc, s0, v3
	s_and_b64 exec, exec, vcc
	s_cbranch_execz .Lmy_pf_a
	s_waitcnt vmcnt(0)
	v_lshlrev_b32_e32 v8, 2, v8
	v_add_u32_e32 v8, 0x20840, v8
	ds_read_b32 v8, v8
	s_add_u32 s6, s16, 0x2bc10000
	s_addc_u32 s7, s17, 0
	s_waitcnt lgkmcnt(0)
	v_add_u32_e32 v9, v9, v8
	global_store_dword v7, v9, s[6:7]
.Lmy_pf_a:
	s_or_b64 exec, exec, s[2:3]
	s_lshl_b32 s4, s18, 3
	s_cmp_ge_i32 s97, s4
	v_readfirstlane_b32 s19, v2
	s_waitcnt lgkmcnt(0)
	s_barrier
	s_cbranch_scc1 .LBB0_1591
	v_ashrrev_i32_e32 v1, 31, v2
	v_lshrrev_b32_e32 v1, 26, v1
	v_add_u32_e32 v1, v2, v1
	v_ashrrev_i32_e32 v4, 6, v1
	v_bfe_i32 v1, v2, 27, 1
	v_lshlrev_b32_e32 v3, 4, v2
	v_lshrrev_b32_e32 v1, 22, v1
	v_add_u32_e32 v1, v3, v1
	v_and_b32_e32 v1, 0xfffffc00, v1
	v_sub_u32_e32 v1, v3, v1
	v_lshrrev_b32_e32 v5, 4, v1
	v_bitop3_b32 v5, v5, v1, 32 bitop3:0x6c
	v_ashrrev_i32_e32 v6, 31, v5
	v_lshrrev_b32_e32 v6, 26, v6
	v_add_u32_e32 v6, v5, v6
	v_ashrrev_i32_e32 v7, 6, v6
	v_and_b32_e32 v6, 0xc0, v6
	v_sub_u32_e32 v5, v5, v6
	v_lshlrev_b32_e32 v1, 3, v4
	v_lshlrev_b32_e32 v4, 5, v4
	v_ashrrev_i16_sdwa v5, v250, sext(v5) dst_sel:DWORD dst_unused:UNUSED_PAD src0_sel:DWORD src1_sel:BYTE_0
	v_and_b32_e32 v4, 32, v4
	v_bfe_i32 v5, v5, 0, 16
	v_add_u32_e32 v3, 0x2000, v3
	v_readlane_b32 s0, v255, 37
	v_add_lshl_u32 v219, v4, v5, 1
	v_ashrrev_i32_e32 v4, 31, v3
	s_add_u32 s6, s16, 0x4578000
	v_readlane_b32 s1, v255, 38
	v_lshrrev_b32_e32 v4, 22, v4
	s_addc_u32 s7, s17, 0
	s_lshl_b64 s[0:1], s[0:1], 26
	v_add_u32_e32 v4, v3, v4
	s_add_u32 s0, s16, s0
	v_and_b32_e32 v1, -16, v1
	v_ashrrev_i32_e32 v4, 10, v4
	s_addc_u32 s1, s17, s1
	v_add_u32_e32 v1, v7, v1
	v_mul_i32_i24_e32 v5, 0x400, v4
	s_add_u32 s22, s0, 0x40eec000
	v_lshlrev_b32_e32 v6, 1, v1
	v_lshrrev_b32_e32 v8, 2, v1
	v_and_b32_e32 v7, 3, v7
	s_mov_b32 s0, 0x3fffe0
	v_sub_u32_e32 v3, v3, v5
	v_and_b32_e32 v6, 24, v6
	v_and_b32_e32 v8, 4, v8
	v_and_or_b32 v7, v1, s0, v7
	v_lshrrev_b32_e32 v5, 4, v3
	v_or3_b32 v6, v7, v8, v6
	v_bitop3_b32 v3, v5, v3, 32 bitop3:0x6c
	v_lshl_add_u32 v170, v6, 10, v219
	v_ashrrev_i32_e32 v6, 31, v3
	v_lshrrev_b32_e32 v6, 26, v6
	v_lshlrev_b32_e32 v5, 3, v4
	v_add_u32_e32 v6, v3, v6
	s_addc_u32 s23, s1, 0
	v_and_b32_e32 v5, -16, v5
	v_ashrrev_i32_e32 v7, 6, v6
	s_add_u32 s28, s16, 0xd5f8000
	v_add_u32_e32 v236, v7, v5
	v_and_b32_e32 v7, 3, v7
	s_addc_u32 s29, s17, 0
	v_and_or_b32 v7, v236, s0, v7
	s_ashr_i32 s0, s19, 6
	v_readlane_b32 s2, v254, 11
	s_add_i32 s24, s18, 1
	s_ashr_i32 s1, s19, 8
	s_lshl_b32 s25, s0, 10
	v_readlane_b32 s3, v254, 12
	s_and_b64 s[2:3], s[2:3], exec
	s_cselect_b32 s2, s24, s18
	v_readlane_b32 s3, v254, 16
	s_mul_i32 s2, s2, s3
	v_readlane_b32 s3, v254, 17
	s_add_i32 s2, s2, s3
	s_ashr_i32 s3, s2, 31
	s_lshr_b32 s3, s3, 26
	s_add_i32 s3, s2, s3
	s_ashr_i32 s5, s3, 6
	v_and_b32_e32 v5, 0xc0, v6
	s_lshl_b32 s5, s5, 3
	v_sub_u32_e32 v3, v3, v5
	s_sub_i32 s8, s18, s5
	v_lshlrev_b32_e32 v4, 5, v4
	v_ashrrev_i16_sdwa v3, v250, sext(v3) dst_sel:DWORD dst_unused:UNUSED_PAD src0_sel:DWORD src1_sel:BYTE_0
	s_min_i32 s8, s8, 8
	v_and_b32_e32 v4, 32, v4
	v_bfe_i32 v3, v3, 0, 16
	s_abs_i32 s10, s8
	v_add_lshl_u32 v212, v4, v3, 1
	v_cvt_f32_u32_e32 v3, s10
	s_sub_i32 s11, 0, s10
	s_andn2_b32 s3, s3, 63
	s_sub_i32 s2, s2, s3
	v_rcp_iflag_f32_e32 v3, v3
	s_abs_i32 s9, s2
	s_xor_b32 s3, s2, s8
	s_ashr_i32 s3, s3, 31
	v_mul_f32_e32 v3, 0x4f7ffffe, v3
	v_cvt_u32_f32_e32 v3, v3
	v_lshlrev_b32_e32 v5, 1, v236
	v_lshrrev_b32_e32 v6, 2, v236
	v_and_b32_e32 v5, 24, v5
	v_readfirstlane_b32 s14, v3
	s_mul_i32 s11, s11, s14
	s_mul_hi_u32 s11, s14, s11
	s_add_i32 s14, s14, s11
	s_mul_hi_u32 s11, s9, s14
	s_mul_i32 s14, s11, s10
	s_sub_i32 s9, s9, s14
	s_add_i32 s14, s11, 1
	s_sub_i32 s15, s9, s10
	s_cmp_ge_u32 s9, s10
	s_cselect_b32 s11, s14, s11
	s_cselect_b32 s9, s15, s9
	s_add_i32 s14, s11, 1
	s_cmp_ge_u32 s9, s10
	s_cselect_b32 s9, s14, s11
	s_xor_b32 s9, s9, s3
	s_sub_i32 s53, s9, s3
	s_mul_i32 s3, s53, s8
	s_sub_i32 s2, s2, s3
	s_add_i32 s52, s5, s2
	s_lshl_b32 s2, s52, 2
	s_add_i32 s2, s2, 0
	s_add_i32 s2, s2, 0x20000
	v_mov_b32_e32 v3, s2
	ds_read_b32 v3, v3
	v_and_b32_e32 v6, 4, v6
	v_or3_b32 v5, v7, v6, v5
	v_lshl_add_u32 v172, v5, 10, v212
	v_mov_b32_e32 v171, v35
	s_waitcnt lgkmcnt(0)
	v_readfirstlane_b32 s2, v3
	s_lshr_b32 s100, s2, 8
	s_and_b32 s2, s2, 0xff
	s_lshl_b32 s2, s2, 3
	s_add_i32 s8, s2, s53
	s_lshl_b32 s2, s52, 8
	s_lshl_b32 s100, s100, 8
	s_add_i32 s2, s2, s100
	v_add_u32_e32 v4, s2, v1
	v_ashrrev_i32_e32 v5, 31, v4
	v_lshl_add_u64 v[4:5], v[4:5], 2, s[28:29]
	global_load_dword v68, v[4:5], off
	v_add_u32_e32 v4, s2, v236
	v_ashrrev_i32_e32 v5, 31, v4
	v_lshl_add_u64 v[4:5], v[4:5], 2, s[28:29]
	global_load_dword v69, v[4:5], off
	s_bitset1_b32 s2, 7
	v_add_u32_e32 v4, s2, v1
	v_ashrrev_i32_e32 v5, 31, v4
	v_lshl_add_u64 v[4:5], v[4:5], 2, s[28:29]
	global_load_dword v70, v[4:5], off
	v_add_u32_e32 v4, s2, v236
	v_ashrrev_i32_e32 v5, 31, v4
	v_lshl_add_u64 v[4:5], v[4:5], 2, s[28:29]
	global_load_dword v71, v[4:5], off
	s_ashr_i32 s9, s8, 31
	v_mov_b32_e32 v173, v35
	s_lshl_b64 s[2:3], s[8:9], 18
	s_add_u32 s10, s22, s2
	s_addc_u32 s11, s23, s3
	s_add_i32 s9, s25, 0
	s_add_i32 m0, s9, 0x10000
	s_add_i32 s26, s9, 0x2000
	global_load_lds_dwordx4 v170, s[10:11]
	s_add_i32 m0, s9, 0x12000
	s_add_u32 s2, s10, 0x20000
	global_load_lds_dwordx4 v172, s[10:11]
	s_addc_u32 s3, s11, 0
	s_add_i32 s27, s9, 0x4000
	s_add_i32 s34, s9, 0x6000
	v_lshl_add_u64 v[6:7], s[10:11], 0, v[172:173]
	s_waitcnt vmcnt(2)
	v_min_u32_e32 v68, 0x43ff, v68
	v_min_u32_e32 v69, 0x43ff, v69
	v_min_u32_e32 v70, 0x43ff, v70
	v_min_u32_e32 v71, 0x43ff, v71
	v_lshl_add_u32 v174, v68, 10, v219
	v_lshl_add_u32 v176, v69, 10, v212
	v_lshl_add_u32 v178, v70, 10, v219
	v_lshl_add_u32 v180, v71, 10, v212
	s_mov_b32 m0, s9
	s_nop 0
	global_load_lds_dwordx4 v174, s[6:7]
	s_mov_b32 m0, s26
	s_nop 0
	global_load_lds_dwordx4 v176, s[6:7]
	s_add_i32 m0, s9, 0x14000
	s_nop 0
	global_load_lds_dwordx4 v170, s[2:3]
	s_add_i32 m0, s9, 0x16000
	s_nop 0
	global_load_lds_dwordx4 v172, s[2:3]
	s_mov_b32 m0, s27
	v_lshl_add_u64 v[4:5], s[10:11], 0, v[170:171]
	global_load_lds_dwordx4 v178, s[6:7]
	s_mov_b32 m0, s34
	s_cmp_lg_u32 s1, 1
	global_load_lds_dwordx4 v180, s[6:7]
	s_cbranch_scc1 .LBB0_1580
	s_barrier
